# recurrence pass B: the idle wave 4 streams the serial chain's P/Q chunks into L2 ahead of it (loader/consumer cache warming)
# baseline (speedup 1.0000x reference)
; DI void phase_chunkB(const Args& a, LAS unsigned char* lds, int wave, int lane, int bid, int G) {
;     ...
;     for (int u = bid; u < NB * NH * 4; u += G) { const int iq = u & 3, bh = u >> 2;
;         bf16x8 pf[3][4][2]; f32x4 qv[3][4];
; __global__ void __launch_bounds__(NTHR, 2) mk_fwd(ArgsV argsv) {
;     ...
;             { PH_BEGIN(); phase_chunkB(a, lds, wave, lane, bid, G); if (wave != 0 && wave != 4 && l == 0) phase_convert<1>(a, 0, lds, bid * (NWAVES - 2) + (wave < 4 ? wave - 1 : wave - 2), G * (NWAVES - 2), wave, lane); }
.LBB0_1158:
	s_cmpk_lg_i32 s2, 0x100
	s_cbranch_scc1 .Lcbh_skip
	v_and_b32_e32 v8, 63, v0
	v_lshlrev_b32_e32 v9, 4, v8
	v_add_u32_e32 v10, 0x1000, v9
	v_lshrrev_b32_e32 v11, 2, v8
	v_and_b32_e32 v12, 3, v8
	v_lshlrev_b32_e32 v12, 4, v12
	v_lshl_or_b32 v11, v11, 8, v12
	v_add_u32_e32 v12, 0x1000, v11
	v_add_u32_e32 v13, 0x2000, v11
	v_add_u32_e32 v50, 0x3000, v11
	s_mov_b32 s28, s1
.Lcbh_unit:
	s_cmpk_gt_i32 s28, 0xff
	s_cbranch_scc1 .Lcbh_done
	s_ashr_i32 s3, s28, 2
	s_and_b32 s4, s28, 3
	s_mul_i32 s24, s3, 0x42000
	s_add_u32 s32, s8, s24
	s_addc_u32 s33, s9, 0
	s_add_u32 s32, s32, 0x27e31000
	s_addc_u32 s33, s33, 0
	s_mul_i32 s24, s3, 0x84000
	s_lshl_b32 s4, s4, 6
	s_add_u32 s24, s24, s4
	s_add_u32 s34, s8, s24
	s_addc_u32 s35, s9, 0
	s_add_u32 s34, s34, 0x28eb1000
	s_addc_u32 s35, s35, 0
	s_mov_b32 s29, 32
.Lcbh_step:
	global_load_dwordx4 v[2:5], v9, s[32:33]
	global_load_dwordx4 v[2:5], v9, s[32:33] offset:1024
	global_load_dwordx4 v[2:5], v9, s[32:33] offset:2048
	global_load_dwordx4 v[2:5], v9, s[32:33] offset:3072
	global_load_dwordx4 v[2:5], v10, s[32:33]
	global_load_dwordx4 v[2:5], v10, s[32:33] offset:1024
	global_load_dwordx4 v[2:5], v10, s[32:33] offset:2048
	global_load_dwordx4 v[2:5], v10, s[32:33] offset:3072
	global_load_dwordx4 v[2:5], v11, s[34:35]
	global_load_dwordx4 v[2:5], v12, s[34:35]
	global_load_dwordx4 v[2:5], v13, s[34:35]
	global_load_dwordx4 v[2:5], v50, s[34:35]
	s_add_u32 s32, s32, 0x2000
	s_addc_u32 s33, s33, 0
	s_add_u32 s34, s34, 0x4000
	s_addc_u32 s35, s35, 0
	s_waitcnt vmcnt(12)
	s_sub_i32 s29, s29, 1
	s_cmp_lg_u32 s29, 0
	s_cbranch_scc1 .Lcbh_step
	s_add_i32 s28, s28, s0
	s_branch .Lcbh_unit
.Lcbh_done:
	s_waitcnt vmcnt(0)
.Lcbh_skip:
	s_ashr_i32 s3, s2, 6
	s_cmp_gt_u32 s2, 63
	s_cselect_b64 s[4:5], -1, 0
	s_cmp_lg_u32 s3, 4
	s_cselect_b64 s[24:25], -1, 0
	s_and_b64 s[4:5], s[4:5], s[24:25]
	v_readlane_b32 s24, v254, 1
	v_readlane_b32 s25, v254, 2
	s_and_b64 s[4:5], s[24:25], s[4:5]
	s_andn2_b64 vcc, exec, s[4:5]
	s_cbranch_vccnz .LBB0_1258
	s_cmp_lt_i32 s3, 4
	s_cselect_b32 s2, -1, -2
	s_mul_i32 s1, s1, 6
	s_add_i32 s2, s2, s3
	s_add_i32 s1, s2, s1
	s_cmpk_gt_i32 s1, 0x105f
	s_cbranch_scc1 .LBB0_1258
	s_and_b32 s5, s2, 1
	s_add_u32 s24, s12, 0xc8
	s_addc_u32 s25, s13, 0
	s_add_u32 s26, s8, 0x40697200
	s_addc_u32 s27, s9, 0
	s_add_u32 s28, s12, 0xd8
	s_addc_u32 s29, s13, 0
	s_add_u32 s30, s8, 0x4069f200
	s_addc_u32 s31, s9, 0
	s_add_u32 s34, s12, 0xb8
	s_addc_u32 s35, s13, 0
	s_add_u32 s36, s8, 0x3f697200
	s_addc_u32 s37, s9, 0
	s_add_u32 s40, s12, 0xb0
	s_addc_u32 s41, s13, 0
	s_add_u32 s42, s8, 0x3ee97200
	s_addc_u32 s43, s9, 0
	s_add_u32 s12, s12, 0xa8
	s_addc_u32 s13, s13, 0
	s_waitcnt vmcnt(31)
	v_lshlrev_b32_e32 v2, 2, v177
	s_add_u32 s8, s8, 0x3e697200
	s_mul_i32 s4, s0, 6
	s_waitcnt vmcnt(13)
	v_and_b32_e32 v74, 56, v173
	v_and_b32_e32 v75, 28, v2
	s_mul_i32 s0, s0, 12
	s_addc_u32 s9, s9, 0
	s_branch .LBB0_1162
